# baseline (speedup 1.0000x reference)
_Z11attn_kernelPKhS0_S0_PKfS2_PhPfS4_:
	s_load_dwordx8 s[4:11], s[0:1], 0x0
	s_load_dwordx2 s[18:19], s[0:1], 0x20
	s_bfe_u32 s20, s2, 0x20001
	s_and_b32 s29, s2, 1
	s_lshl_b32 s2, s2, 4
	v_readfirstlane_b32 s28, v0
	s_and_b32 s16, s2, 0xffffff80
	s_lshr_b32 s12, s28, 6
	s_bfe_u32 s22, s28, 0x20006
	s_lshl_b32 s30, s20, 12
	s_lshl_b32 s13, s20, 6
	s_lshl_b32 s14, s29, 5
	s_ashr_i32 s17, s16, 31
	s_lshl_b32 s2, s20, 14
	s_waitcnt lgkmcnt(0)
	s_add_u32 s2, s10, s2
	s_addc_u32 s3, s11, 0
	s_lshl_b64 s[10:11], s[16:17], 2
	s_add_u32 s2, s2, s10
	s_addc_u32 s3, s3, s11
	s_lshl_b32 s15, s22, 7
	v_and_b32_e32 v1, 31, v0
	s_add_u32 s2, s2, s15
	s_addc_u32 s3, s3, 0
	v_lshlrev_b32_e32 v169, 2, v1
	global_load_dword v168, v169, s[2:3]
	s_or_b32 s2, s13, s14
	v_or_b32_e32 v2, s2, v1
	s_ashr_i32 s2, s16, 6
	s_ashr_i32 s3, s2, 31
	s_add_u32 s2, s13, s2
	s_addc_u32 s3, 0, s3
	s_bfe_u32 s15, s12, 0x10001
	s_or_b32 s2, s2, s15
	s_lshl_b64 s[2:3], s[2:3], 14
	s_add_u32 s2, s4, s2
	s_addc_u32 s3, s5, s3
	s_lshl_b32 s21, s12, 10
	s_and_b32 s4, s21, 0x400
	v_and_b32_e32 v198, 63, v0
	v_lshlrev_b32_e32 v2, 2, v2
	s_add_u32 s2, s2, s4
	v_mov_b32_e32 v3, 0
	global_load_dword v182, v2, s[18:19]
	s_addc_u32 s3, s3, 0
	v_lshlrev_b32_e32 v2, 4, v198
	v_lshl_add_u64 v[4:5], s[2:3], 0, v[2:3]
	global_load_dwordx4 v[132:135], v2, s[2:3]
	global_load_dwordx4 v[136:139], v2, s[2:3] offset:2048
	s_movk_i32 s2, 0x1000
	v_add_co_u32_e32 v6, vcc, s2, v4
	s_nop 1
	v_addc_co_u32_e32 v7, vcc, 0, v5, vcc
	global_load_dwordx4 v[140:143], v[6:7], off
	global_load_dwordx4 v[144:147], v[6:7], off offset:2048
	v_add_co_u32_e32 v6, vcc, 0x2000, v4
	s_nop 1
	v_addc_co_u32_e32 v7, vcc, 0, v5, vcc
	v_add_co_u32_e32 v4, vcc, 0x3000, v4
	global_load_dwordx4 v[148:151], v[6:7], off
	global_load_dwordx4 v[152:155], v[6:7], off offset:2048
	v_addc_co_u32_e32 v5, vcc, 0, v5, vcc
	global_load_dwordx4 v[156:159], v[4:5], off
	global_load_dwordx4 v[160:163], v[4:5], off offset:2048
	v_cmp_eq_u32_e32 vcc, 0, v0
	s_and_saveexec_b64 s[2:3], vcc
	s_add_i32 s4, 0, 0x1cc00
	v_mov_b32_e32 v4, s4
	ds_write_b32 v4, v3
	s_or_b64 exec, exec, s[2:3]
	s_lshl_b32 s23, s29, 19
	s_lshl_b32 s2, s30, 8
	s_or_b32 s3, s13, s14
	s_or_b32 s2, s23, s2
	s_lshl_b32 s4, s3, 14
	s_lshr_b32 s34, s28, 8
	s_add_u32 s2, s6, s2
	s_addc_u32 s3, s7, 0
	s_add_u32 s14, s8, s4
	s_addc_u32 s15, s9, 0
	v_lshrrev_b32_e32 v3, 4, v198
	s_lshl_b32 s4, s12, 2
	v_bitop3_b32 v4, s4, v0, v3 bitop3:0x36
	v_lshlrev_b32_e32 v4, 4, v4
	v_and_b32_e32 v18, 0x3c0, v2
	v_xor_b32_e32 v2, v3, v0
	v_lshlrev_b32_e32 v20, 8, v3
	v_and_b32_e32 v21, 0xf0, v4
	v_lshlrev_b32_e32 v2, 4, v2
	v_and_b32_e32 v19, 48, v2
	v_or3_b32 v2, v21, v20, s21
	s_add_i32 s31, s21, 0
	v_ashrrev_i32_e32 v3, 31, v2
	s_add_i32 s36, s31, 0xc000
	v_lshl_add_u64 v[174:175], s[2:3], 0, v[2:3]
	s_mov_b32 m0, s36
	s_mov_b64 s[12:13], 0x2000
	s_add_i32 s35, s31, 0xe000
	global_load_lds_dwordx4 v[174:175], off
	v_lshl_add_u64 v[176:177], v[174:175], 0, s[12:13]
	s_mov_b32 m0, s35
	s_mov_b64 s[2:3], 0x4000
	v_or3_b32 v4, v19, v18, s21
	global_load_lds_dwordx4 v[176:177], off
	v_lshl_add_u64 v[2:3], v[174:175], 0, s[2:3]
	s_add_i32 m0, s31, 0x10000
	s_mov_b64 s[4:5], 0x6000
	global_load_lds_dwordx4 v[2:3], off
	v_lshl_add_u64 v[2:3], v[174:175], 0, s[4:5]
	s_add_i32 m0, s31, 0x12000
	v_ashrrev_i32_e32 v5, 31, v4
	global_load_lds_dwordx4 v[2:3], off
	v_lshl_add_u64 v[178:179], s[14:15], 0, v[4:5]
	s_mov_b32 m0, s31
	s_add_i32 s37, s31, 0x2000
	global_load_lds_dwordx4 v[178:179], off
	v_lshl_add_u64 v[180:181], v[178:179], 0, s[12:13]
	s_mov_b32 m0, s37
	v_lshrrev_b32_e32 v183, 5, v198
	global_load_lds_dwordx4 v[180:181], off
	s_lshl_b32 s24, s34, 13
	s_add_i32 s12, s24, 0
	v_and_b32_e32 v2, 15, v0
	v_bitop3_b32 v3, v183, v0, 15 bitop3:0x78
	v_lshl_add_u32 v184, v1, 8, s12
	v_lshlrev_b32_e32 v185, 4, v3
	v_bitop3_b32 v4, v183, v2, 2 bitop3:0x36
	s_waitcnt vmcnt(4) lgkmcnt(0)
	s_barrier
	v_add_u32_e32 v3, v184, v185
	v_lshlrev_b32_e32 v186, 4, v4
	v_add_u32_e32 v4, v184, v186
	ds_read_b128 v[22:25], v3 offset:49152
	ds_read_b128 v[26:29], v4 offset:49152
	v_bitop3_b32 v3, v183, v2, 4 bitop3:0x36
	v_lshlrev_b32_e32 v187, 4, v3
	v_bitop3_b32 v4, v183, v2, 6 bitop3:0x36
	v_add_u32_e32 v3, v184, v187
	v_lshlrev_b32_e32 v188, 4, v4
	v_add_u32_e32 v4, v184, v188
	ds_read_b128 v[30:33], v3 offset:49152
	ds_read_b128 v[34:37], v4 offset:49152
	v_bitop3_b32 v3, v183, v2, 8 bitop3:0x36
	v_lshlrev_b32_e32 v189, 4, v3
	v_bitop3_b32 v4, v183, v2, 10 bitop3:0x36
	v_add_u32_e32 v3, v184, v189
	v_lshlrev_b32_e32 v190, 4, v4
	v_add_u32_e32 v4, v184, v190
	ds_read_b128 v[38:41], v3 offset:49152
	ds_read_b128 v[42:45], v4 offset:49152
	v_bitop3_b32 v3, v183, v2, 12 bitop3:0x36
	v_lshlrev_b32_e32 v191, 4, v3
	v_bitop3_b32 v2, v183, v2, 14 bitop3:0x36
	v_add_u32_e32 v3, v184, v191
	v_lshlrev_b32_e32 v192, 4, v2
	v_add_u32_e32 v2, v184, v192
	ds_read_b128 v[46:49], v3 offset:49152
	ds_read_b128 v[50:53], v2 offset:49152
	v_mov_b32_e32 v2, 0x4b400000
	v_mov_b32_e32 v3, v2
	v_mov_b32_e32 v4, v2
	v_mov_b32_e32 v5, v2
	v_mov_b32_e32 v6, v2
	v_mov_b32_e32 v7, v2
	v_mov_b32_e32 v8, v2
	v_mov_b32_e32 v9, v2
	v_mov_b32_e32 v10, v2
	v_mov_b32_e32 v11, v2
	v_mov_b32_e32 v12, v2
	v_mov_b32_e32 v13, v2
	v_mov_b32_e32 v14, v2
	v_mov_b32_e32 v15, v2
	v_mov_b32_e32 v16, v2
	v_mov_b32_e32 v17, v2
	s_mov_b64 s[12:13], 0x8000
	s_add_i32 m0, s31, 0x14000
	s_waitcnt vmcnt(4) lgkmcnt(0)
	v_mfma_i32_32x32x32_i8 v[2:17], v[22:25], v[132:135], v[2:17]
	v_lshl_add_u64 v[22:23], v[174:175], 0, s[12:13]
	s_mov_b64 s[12:13], 0xa000
	v_lshl_add_u64 v[24:25], v[174:175], 0, s[12:13]
	global_load_lds_dwordx4 v[22:23], off
	s_add_i32 m0, s31, 0x16000
	v_lshl_add_u64 v[22:23], v[178:179], 0, s[2:3]
	global_load_lds_dwordx4 v[24:25], off
	s_add_i32 m0, s31, 0x4000
	v_lshl_add_u64 v[24:25], v[178:179], 0, s[4:5]
	global_load_lds_dwordx4 v[22:23], off
	s_add_i32 m0, s31, 0x6000
	v_mfma_i32_32x32x32_i8 v[2:17], v[26:29], v[136:139], v[2:17]
	global_load_lds_dwordx4 v[24:25], off
	v_readlane_b32 s2, v182, 0
	v_cmp_lt_u32_e32 vcc, 31, v198
	s_nop 0
	v_mul_f32_e32 v22, s2, v168
	v_mfma_i32_32x32x32_i8 v[2:17], v[30:33], v[140:143], v[2:17]
	v_cmp_gt_u32_e64 s[2:3], 32, v198
	v_mfma_i32_32x32x32_i8 v[2:17], v[34:37], v[144:147], v[2:17]
	v_mfma_i32_32x32x32_i8 v[2:17], v[38:41], v[148:151], v[2:17]
	v_mfma_i32_32x32x32_i8 v[2:17], v[42:45], v[152:155], v[2:17]
	v_mfma_i32_32x32x32_i8 v[2:17], v[46:49], v[156:159], v[2:17]
	v_mfma_i32_32x32x32_i8 v[2:17], v[50:53], v[160:163], v[2:17]
	s_nop 11
	v_max_i32_e32 v23, v2, v3
	v_max3_i32 v23, v23, v4, v5
	v_max3_i32 v23, v23, v6, v7
	v_max3_i32 v23, v23, v8, v9
	v_max3_i32 v23, v23, v10, v11
	v_max3_i32 v23, v23, v12, v13
	v_max3_i32 v23, v23, v14, v15
	v_max3_i32 v23, v23, v16, v17
	v_mov_b32_e32 v24, v23
	s_nop 1
	v_permlane32_swap_b32_e32 v23, v24
	v_max_i32_e32 v23, v23, v24
	v_add_f32_e32 v24, 0xcb400000, v23
	v_lshl_or_b32 v23, s34, 5, v1
	s_and_saveexec_b64 s[4:5], vcc
	s_xor_b64 s[4:5], exec, s[4:5]
	s_lshl_b32 s25, s22, 6
	v_lshl_or_b32 v23, s34, 5, v1
	s_or_saveexec_b64 s[18:19], s[4:5]
	s_load_dwordx4 s[12:15], s[0:1], 0x28
	s_load_dwordx2 s[4:5], s[0:1], 0x38
	s_lshl_b32 s33, s22, 5
	v_mul_f32_e32 v24, v22, v24
	v_mov_b32_e32 v25, s25
	s_xor_b64 exec, exec, s[18:19]
	s_cbranch_execz .LBB2_6
	s_lshl_b32 s1, s22, 8
	s_add_i32 s1, s1, 0
	v_lshl_add_u32 v25, v23, 2, s1
	s_lshl_b32 s0, s22, 6
	v_add_u32_e32 v25, 0x1c000, v25
	ds_write_b32 v25, v24
	v_mov_b32_e32 v25, s0
